# P11 Y/X1 loads nt (on top of P0 loads nt, P1/conv stores nt)
# speedup vs baseline: 1.0173x; 1.0008x over previous
.LBB0_1286:
	s_add_u32 s0, s92, s8
	s_addc_u32 s1, s93, s9
	v_lshl_add_u64 v[24:25], s[92:93], 0, v[18:19]
	global_load_dwordx4 v[40:43], v36, s[0:1]
	v_add_co_u32_e32 v24, vcc, 0xe000000, v24
	v_mov_b32_e32 v27, v23
	s_nop 0
	v_addc_co_u32_e32 v25, vcc, 0, v25, vcc
	global_load_dwordx2 v[44:45], v[24:25], off offset:512 nt
	global_load_dwordx2 v[46:47], v[24:25], off offset:1024 nt
	global_load_dwordx2 v[48:49], v[24:25], off offset:1536 nt
	global_load_dwordx2 v[50:51], v[24:25], off nt
	v_mov_b32_e32 v29, v23
	s_add_i32 s2, s2, s4
	s_add_u32 s8, s8, s10
	s_addc_u32 s9, s9, s11
	v_lshl_add_u64 v[18:19], v[18:19], 0, s[6:7]
	s_cmp_lt_i32 s2, 0x8000
	s_waitcnt vmcnt(4)
	v_ashrrev_i32_e32 v25, 31, v40
	v_mov_b32_e32 v24, v40
	v_ashrrev_i32_e32 v53, 31, v41
	v_mov_b32_e32 v52, v41
	v_ashrrev_i32_e32 v41, 31, v42
	v_mov_b32_e32 v40, v42
	v_ashrrev_i32_e32 v55, 31, v43
	v_mov_b32_e32 v54, v43
	v_lshlrev_b64 v[24:25], 10, v[24:25]
	s_waitcnt vmcnt(1)
	v_lshlrev_b32_e32 v28, 16, v48
	v_and_b32_e32 v59, 0xffff0000, v48
	v_lshlrev_b32_e32 v43, 16, v49
	v_and_b32_e32 v57, 0xffff0000, v49
	v_lshlrev_b64 v[48:49], 10, v[52:53]
	v_lshlrev_b64 v[52:53], 10, v[54:55]
	v_lshlrev_b64 v[40:41], 10, v[40:41]
	v_lshl_add_u64 v[24:25], v[16:17], 0, v[24:25]
	v_lshl_add_u64 v[48:49], v[16:17], 0, v[48:49]
	v_lshl_add_u64 v[40:41], v[16:17], 0, v[40:41]
	v_lshl_add_u64 v[52:53], v[16:17], 0, v[52:53]
	global_load_dword v39, v[24:25], off nt
	global_load_dword v58, v[24:25], off offset:256 nt
	global_load_dword v61, v[24:25], off offset:512 nt
	global_load_dword v63, v[24:25], off offset:768 nt
	global_load_dword v65, v[48:49], off nt
	global_load_dword v67, v[48:49], off offset:256 nt
	global_load_dword v68, v[48:49], off offset:512 nt
	global_load_dword v79, v[48:49], off offset:768 nt
	global_load_dword v80, v[40:41], off nt
	global_load_dword v82, v[40:41], off offset:256 nt
	global_load_dword v91, v[40:41], off offset:512 nt
	global_load_dword v93, v[40:41], off offset:768 nt
	global_load_dword v95, v[52:53], off nt
	global_load_dword v97, v[52:53], off offset:256 nt
	global_load_dword v99, v[52:53], off offset:512 nt
	global_load_dword v108, v[52:53], off offset:768 nt
	s_waitcnt vmcnt(16)
	v_lshlrev_b32_e32 v54, 16, v50
	v_and_b32_e32 v55, 0xffff0000, v50
	v_lshlrev_b32_e32 v50, 16, v51
	v_and_b32_e32 v51, 0xffff0000, v51
	v_lshlrev_b32_e32 v22, 16, v44
	v_and_b32_e32 v26, 0xffff0000, v45
	v_lshlrev_b32_e32 v56, 16, v47
	v_lshlrev_b32_e32 v42, 16, v46
	v_and_b32_e32 v44, 0xffff0000, v44
	v_lshlrev_b32_e32 v45, 16, v45
	v_and_b32_e32 v47, 0xffff0000, v47
	v_and_b32_e32 v46, 0xffff0000, v46
	s_waitcnt vmcnt(15)
	v_cvt_f32_fp8_e32 v24, v39
	v_cvt_f32_fp8_sdwa v25, v39 src0_sel:BYTE_1
	v_cvt_f32_fp8_sdwa v40, v39 src0_sel:BYTE_2
	v_cvt_f32_fp8_sdwa v41, v39 src0_sel:BYTE_3
	s_waitcnt vmcnt(14)
	v_cvt_f32_fp8_e32 v48, v58
	v_cvt_f32_fp8_sdwa v52, v58 src0_sel:BYTE_1
	v_cvt_f32_fp8_sdwa v60, v58 src0_sel:BYTE_2
	v_cvt_f32_fp8_sdwa v62, v58 src0_sel:BYTE_3
	s_waitcnt vmcnt(13)
	v_cvt_f32_fp8_e32 v39, v61
	v_cvt_f32_fp8_sdwa v64, v61 src0_sel:BYTE_1
	v_cvt_f32_fp8_sdwa v58, v61 src0_sel:BYTE_2
	v_cvt_f32_fp8_sdwa v66, v61 src0_sel:BYTE_3
	s_waitcnt vmcnt(12)
	v_cvt_f32_fp8_e32 v110, v63
	v_cvt_f32_fp8_sdwa v69, v63 src0_sel:BYTE_1
	v_cvt_f32_fp8_sdwa v71, v63 src0_sel:BYTE_2
	v_cvt_f32_fp8_sdwa v73, v63 src0_sel:BYTE_3
	s_waitcnt vmcnt(10)
	v_cvt_f32_fp8_e32 v49, v67
	v_cvt_f32_fp8_sdwa v53, v67 src0_sel:BYTE_1
	v_cvt_f32_fp8_sdwa v61, v67 src0_sel:BYTE_2
	v_cvt_f32_fp8_sdwa v63, v67 src0_sel:BYTE_3
	v_cvt_f32_fp8_e32 v74, v65
	v_cvt_f32_fp8_sdwa v75, v65 src0_sel:BYTE_1
	v_cvt_f32_fp8_sdwa v76, v65 src0_sel:BYTE_2
	v_cvt_f32_fp8_sdwa v77, v65 src0_sel:BYTE_3
	s_waitcnt vmcnt(9)
	v_cvt_f32_fp8_e32 v70, v68
	v_cvt_f32_fp8_sdwa v65, v68 src0_sel:BYTE_1
	v_cvt_f32_fp8_sdwa v72, v68 src0_sel:BYTE_2
	v_cvt_f32_fp8_sdwa v67, v68 src0_sel:BYTE_3
	s_waitcnt vmcnt(8)
	v_cvt_f32_fp8_e32 v78, v79
	v_cvt_f32_fp8_sdwa v81, v79 src0_sel:BYTE_1
	v_cvt_f32_fp8_sdwa v83, v79 src0_sel:BYTE_2
	v_cvt_f32_fp8_sdwa v85, v79 src0_sel:BYTE_3
	s_waitcnt vmcnt(6)
	v_cvt_f32_fp8_e32 v68, v82
	v_cvt_f32_fp8_sdwa v90, v82 src0_sel:BYTE_1
	v_cvt_f32_fp8_sdwa v92, v82 src0_sel:BYTE_2
	v_cvt_f32_fp8_sdwa v94, v82 src0_sel:BYTE_3
	s_waitcnt vmcnt(5)
	v_cvt_f32_fp8_e32 v82, v91
	v_cvt_f32_fp8_sdwa v96, v91 src0_sel:BYTE_1
	v_cvt_f32_fp8_sdwa v84, v91 src0_sel:BYTE_2
	v_cvt_f32_fp8_sdwa v98, v91 src0_sel:BYTE_3
	s_waitcnt vmcnt(4)
	v_cvt_f32_fp8_e32 v79, v93
	v_cvt_f32_fp8_sdwa v112, v93 src0_sel:BYTE_1
	v_cvt_f32_fp8_sdwa v101, v93 src0_sel:BYTE_2
	v_cvt_f32_fp8_sdwa v103, v93 src0_sel:BYTE_3
	s_waitcnt vmcnt(2)
	v_cvt_f32_fp8_sdwa v91, v97 src0_sel:BYTE_1
	v_cvt_f32_fp8_sdwa v93, v97 src0_sel:BYTE_2
	v_cvt_f32_fp8_e32 v86, v80
	v_cvt_f32_fp8_sdwa v87, v80 src0_sel:BYTE_1
	v_cvt_f32_fp8_sdwa v88, v80 src0_sel:BYTE_2
	v_cvt_f32_fp8_sdwa v89, v80 src0_sel:BYTE_3
	v_cvt_f32_fp8_e32 v104, v95
	v_cvt_f32_fp8_sdwa v105, v95 src0_sel:BYTE_1
	v_cvt_f32_fp8_sdwa v106, v95 src0_sel:BYTE_2
	v_cvt_f32_fp8_sdwa v107, v95 src0_sel:BYTE_3
	v_cvt_f32_fp8_sdwa v95, v97 src0_sel:BYTE_3
	v_cvt_f32_fp8_e32 v80, v97
	s_waitcnt vmcnt(1)
	v_cvt_f32_fp8_e32 v100, v99
	v_cvt_f32_fp8_sdwa v97, v99 src0_sel:BYTE_1
	v_cvt_f32_fp8_sdwa v102, v99 src0_sel:BYTE_2
	v_cvt_f32_fp8_sdwa v99, v99 src0_sel:BYTE_3
	s_waitcnt vmcnt(0)
	v_cvt_f32_fp8_e32 v109, v108
	v_cvt_f32_fp8_sdwa v111, v108 src0_sel:BYTE_1
	v_cvt_f32_fp8_sdwa v114, v108 src0_sel:BYTE_2
	v_cvt_f32_fp8_sdwa v108, v108 src0_sel:BYTE_3
	v_pk_mul_f32 v[48:49], v[48:49], s[14:15] op_sel_hi:[1,0]
	v_pk_mul_f32 v[52:53], v[52:53], s[14:15] op_sel_hi:[1,0]
	v_pk_mul_f32 v[60:61], v[60:61], s[14:15] op_sel_hi:[1,0]
	v_pk_mul_f32 v[62:63], v[62:63], s[14:15] op_sel_hi:[1,0]
	v_pk_fma_f32 v[24:25], v[24:25], s[14:15], v[54:55] op_sel_hi:[1,0,1]
	v_pk_fma_f32 v[40:41], v[40:41], s[14:15], v[50:51] op_sel_hi:[1,0,1]
	v_fmac_f32_e32 v56, 0x3d800000, v58
	v_pk_mul_f32 v[64:65], v[64:65], s[14:15] op_sel_hi:[1,0]
	v_pk_mul_f32 v[66:67], v[66:67], s[14:15] op_sel_hi:[1,0]
	v_pk_mul_f32 v[50:51], v[90:91], s[14:15] op_sel_hi:[1,0]
	v_pk_mul_f32 v[54:55], v[92:93], s[14:15] op_sel_hi:[1,0]
	v_add_f32_e32 v22, v48, v22
	v_add_f32_e32 v26, v62, v26
	v_pk_fma_f32 v[24:25], v[74:75], s[14:15], v[24:25] op_sel_hi:[1,0,1]
	v_pk_fma_f32 v[40:41], v[76:77], s[14:15], v[40:41] op_sel_hi:[1,0,1]
	v_mov_b32_e32 v74, v52
	v_mov_b32_e32 v75, v60
	v_fmac_f32_e32 v42, 0x3d800000, v39
	v_fmac_f32_e32 v28, 0x3d800000, v110
	v_pk_mul_f32 v[78:79], v[78:79], s[14:15] op_sel_hi:[1,0]
	v_pk_mul_f32 v[90:91], v[94:95], s[14:15] op_sel_hi:[1,0]
	v_mov_b32_e32 v60, v53
	v_mov_b32_e32 v52, v50
	v_mov_b32_e32 v53, v54
	v_mov_b32_e32 v54, v51
	v_mov_b32_e32 v50, v64
	v_mov_b32_e32 v51, v66
	v_pk_fma_f32 v[56:57], v[72:73], s[14:15], v[56:57] op_sel_hi:[1,0,1]
	v_add_f32_e32 v58, v22, v49
	v_add_f32_e32 v22, v26, v63
	v_pk_fma_f32 v[24:25], v[86:87], s[14:15], v[24:25] op_sel_hi:[1,0,1]
	v_pk_fma_f32 v[40:41], v[88:89], s[14:15], v[40:41] op_sel_hi:[1,0,1]
	v_pk_add_f32 v[44:45], v[74:75], v[44:45]
	v_pk_mul_f32 v[92:93], v[96:97], s[14:15] op_sel_hi:[1,0]
	v_pk_mul_f32 v[94:95], v[98:99], s[14:15] op_sel_hi:[1,0]
	v_add_f32_e32 v28, v28, v78
	v_mov_b32_e32 v66, v65
	v_pk_fma_f32 v[42:43], v[70:71], s[14:15], v[42:43] op_sel_hi:[1,0,1]
	v_pk_add_f32 v[46:47], v[50:51], v[46:47]
	v_pk_fma_f32 v[50:51], v[84:85], s[14:15], v[56:57] op_sel_hi:[1,0,1]
	v_pk_fma_f32 v[24:25], v[104:105], s[14:15], v[24:25] op_sel_hi:[1,0,1]
	v_pk_fma_f32 v[40:41], v[106:107], s[14:15], v[40:41] op_sel_hi:[1,0,1]
	v_pk_add_f32 v[44:45], v[44:45], v[60:61]
	v_add_f32_e32 v22, v22, v90
	v_pk_fma_f32 v[56:57], v[68:69], s[14:15], v[58:59] op_sel_hi:[1,0,1]
	v_mul_f32_e32 v99, 0x3d800000, v108
	v_mov_b32_e32 v64, v92
	v_mov_b32_e32 v65, v94
	v_add_f32_e32 v49, v28, v79
	v_pk_fma_f32 v[42:43], v[82:83], s[14:15], v[42:43] op_sel_hi:[1,0,1]
	v_pk_add_f32 v[46:47], v[46:47], v[66:67]
	v_pk_add_f32 v[44:45], v[44:45], v[52:53]
	v_add_f32_e32 v116, v22, v91
	v_pk_mul_f32 v[52:53], v[40:41], v[40:41]
	v_pk_fma_f32 v[56:57], v[80:81], s[14:15], v[56:57] op_sel_hi:[1,0,1]
	v_mov_b32_e32 v108, v24
	v_mov_b32_e32 v22, v24
	v_mul_f32_e32 v48, v25, v25
	v_mul_f32_e32 v113, 0x3d800000, v112
	v_mul_f32_e32 v97, 0x3d800000, v114
	v_mov_b32_e32 v115, v109
	v_mov_b32_e32 v94, v93
	v_pk_fma_f32 v[42:43], v[100:101], s[14:15], v[42:43] op_sel_hi:[1,0,1]
	v_pk_fma_f32 v[50:51], v[102:103], s[14:15], v[50:51] op_sel_hi:[1,0,1]
	v_pk_add_f32 v[46:47], v[46:47], v[64:65]
	v_mov_b32_e32 v114, v40
	v_mov_b32_e32 v26, v40
	v_pk_add_f32 v[44:45], v[44:45], v[54:55]
	v_pk_fma_f32 v[54:55], v[108:109], v[22:23], v[48:49]
	v_mov_b32_e32 v48, v53
	v_mov_b32_e32 v112, v56
	v_mov_b32_e32 v96, v42
	v_mov_b32_e32 v98, v50
	v_pk_add_f32 v[46:47], v[46:47], v[94:95]
	v_pk_mul_f32 v[52:53], v[56:57], v[56:57]
	v_pk_mul_f32 v[64:65], v[44:45], v[44:45]
	v_pk_fma_f32 v[26:27], v[114:115], v[26:27], v[48:49]
	v_pk_add_f32 v[48:49], v[56:57], v[112:113]
	v_mov_b32_e32 v117, v111
	v_mov_b32_e32 v28, v116
	v_pk_add_f32 v[58:59], v[42:43], v[96:97]
	v_pk_add_f32 v[60:61], v[50:51], v[98:99]
	v_pk_mul_f32 v[66:67], v[46:47], v[46:47]
	v_mov_b32_e32 v110, v44
	v_mov_b32_e32 v22, v44
	v_mov_b32_e32 v53, v49
	v_mov_b32_e32 v48, v65
	v_pk_mul_f32 v[68:69], v[58:59], v[58:59]
	v_pk_mul_f32 v[70:71], v[60:61], v[60:61]
	v_mov_b32_e32 v57, v44
	v_mov_b32_e32 v62, v45
	v_mov_b32_e32 v60, v59
	v_pk_add_f32 v[44:45], v[54:55], v[26:27]
	v_pk_mul_f32 v[26:27], v[54:55], v[26:27]
	v_pk_fma_f32 v[58:59], v[42:43], v[42:43], v[66:67]
	v_pk_fma_f32 v[64:65], v[50:51], v[50:51], v[66:67] op_sel:[0,0,1] op_sel_hi:[1,1,0]
	v_mov_b32_e32 v43, v46
	v_mov_b32_e32 v51, v47
	v_pk_fma_f32 v[46:47], v[110:111], v[22:23], v[52:53]
	v_pk_fma_f32 v[28:29], v[116:117], v[28:29], v[48:49]
	v_mov_b32_e32 v45, v27
	v_pk_add_f32 v[26:27], v[46:47], v[28:29]
	v_pk_mul_f32 v[28:29], v[46:47], v[28:29]
	v_mov_b32_e32 v59, v69
	v_mov_b32_e32 v65, v71
	v_mov_b32_e32 v27, v29
	v_pk_add_f32 v[48:49], v[58:59], v[64:65]
	v_pk_add_f32 v[26:27], v[44:45], v[26:27]
	v_mov_b32_e32 v63, v116
	v_pk_add_f32 v[26:27], v[26:27], v[48:49]
	v_mov_b32_e32 v46, v55
	v_add_f32_e32 v22, v26, v27
	ds_bpermute_b32 v26, v30, v22
	s_waitcnt lgkmcnt(0)
	v_add_f32_e32 v22, v22, v26
	ds_bpermute_b32 v26, v31, v22
	s_waitcnt lgkmcnt(0)
	v_add_f32_e32 v22, v22, v26
	ds_bpermute_b32 v26, v32, v22
	s_waitcnt lgkmcnt(0)
	v_add_f32_e32 v22, v22, v26
	ds_bpermute_b32 v26, v33, v22
	s_waitcnt lgkmcnt(0)
	v_add_f32_e32 v22, v22, v26
	ds_bpermute_b32 v26, v34, v22
	s_waitcnt lgkmcnt(0)
	v_add_f32_e32 v22, v22, v26
	ds_bpermute_b32 v26, v35, v22
	s_waitcnt lgkmcnt(0)
	v_add_f32_e32 v22, v22, v26
	v_fmamk_f32 v22, v22, 0x3a800000, v37
	v_mul_f32_e32 v26, 0x4f800000, v22
	v_cmp_gt_f32_e32 vcc, s3, v22
	s_nop 1
	v_cndmask_b32_e32 v22, v22, v26, vcc
	v_sqrt_f32_e32 v26, v22
	s_nop 0
	v_add_u32_e32 v27, -1, v26
	v_add_u32_e32 v28, 1, v26
	v_fma_f32 v29, -v27, v26, v22
	v_fma_f32 v39, -v28, v26, v22
	v_cmp_ge_f32_e64 s[0:1], 0, v29
	s_nop 1
	v_cndmask_b32_e64 v26, v26, v27, s[0:1]
	v_cmp_lt_f32_e64 s[0:1], 0, v39
	s_nop 1
	v_cndmask_b32_e64 v26, v26, v28, s[0:1]
	v_mul_f32_e32 v27, 0x37800000, v26
	v_cndmask_b32_e32 v26, v26, v27, vcc
	v_cmp_class_f32_e32 vcc, v22, v38
	s_nop 1
	v_cndmask_b32_e32 v22, v26, v22, vcc
	v_div_scale_f32 v26, s[0:1], v22, v22, 1.0
	v_rcp_f32_e32 v28, v26
	v_div_scale_f32 v27, vcc, 1.0, v22, 1.0
	v_fma_f32 v29, -v26, v28, 1.0
	v_fmac_f32_e32 v28, v29, v28
	v_mul_f32_e32 v29, v27, v28
	v_fma_f32 v39, -v26, v29, v27
	v_fmac_f32_e32 v29, v39, v28
	v_fma_f32 v26, -v26, v29, v27
	v_div_fmas_f32 v26, v26, v28, v29
	v_div_fixup_f32 v22, v26, v22, 1.0
	v_pk_mul_f32 v[24:25], v[24:25], v[22:23] op_sel_hi:[1,0]
	v_pk_mul_f32 v[26:27], v[40:41], v[22:23] op_sel_hi:[1,0]
	v_pk_mul_f32 v[28:29], v[56:57], v[22:23] op_sel_hi:[1,0]
	v_pk_mul_f32 v[40:41], v[62:63], v[22:23] op_sel_hi:[1,0]
	v_pk_mul_f32 v[44:45], v[42:43], v[22:23] op_sel_hi:[1,0]
	v_pk_mul_f32 v[48:49], v[50:51], v[22:23] op_sel_hi:[1,0]
	v_pk_mul_f32 v[52:53], v[46:47], v[22:23] op_sel_hi:[1,0]
	v_pk_mul_f32 v[50:51], v[60:61], v[22:23] op_sel_hi:[1,0]
	v_pk_mul_f32 v[26:27], v[2:3], v[26:27]
	v_pk_mul_f32 v[24:25], v[0:1], v[24:25]
	v_pk_mul_f32 v[42:43], v[6:7], v[40:41]
	v_pk_mul_f32 v[40:41], v[4:5], v[28:29]
	v_pk_mul_f32 v[46:47], v[10:11], v[48:49]
	v_pk_mul_f32 v[44:45], v[8:9], v[44:45]
	v_pk_mul_f32 v[50:51], v[14:15], v[50:51]
	v_pk_mul_f32 v[48:49], v[12:13], v[52:53]
	global_store_dwordx4 v[20:21], v[24:27], off offset:-3072 nt
	global_store_dwordx4 v[20:21], v[40:43], off offset:-2048 nt
	global_store_dwordx4 v[20:21], v[44:47], off offset:-1024 nt
	global_store_dwordx4 v[20:21], v[48:51], off nt
	v_lshl_add_u64 v[20:21], v[20:21], 0, s[12:13]
	s_cbranch_scc1 .LBB0_1286
